# baseline (speedup 1.0000x reference)
.Lk1_nowarm0:
	s_waitcnt lgkmcnt(0)
	s_add_u32 s8, s4, s17
	s_addc_u32 s9, s5, s20
	s_and_b32 s9, s9, 0xffff
	s_cmp_eq_u32 s21, 9
	s_cselect_b32 s17, 1, 0
	s_cmp_eq_u32 s16, 0
	s_cselect_b32 s17, s17, 0
	s_cmp_lg_u32 s17, 0
	s_cbranch_scc1 .Lk1_warm9

.Lk1_warm9:
	s_mul_i32 s22, s15, 0x3a9800
	v_writelane_b32 v3, s22, 0
	s_add_u32 s23, s22, 0x10000
	v_writelane_b32 v3, s23, 1
	s_add_u32 s22, s22, 0x138800
	v_writelane_b32 v3, s22, 2
	s_add_u32 s23, s22, 0x10000
	v_writelane_b32 v3, s23, 3
	s_add_u32 s22, s22, 0x138800
	v_writelane_b32 v3, s22, 4
	s_add_u32 s23, s22, 0x10000
	v_writelane_b32 v3, s23, 5
	s_mov_b64 exec, 63
	global_load_dword v92, v3, s[32:33]
	s_mul_i32 s22, s15, 0x12c00
	s_add_u32 s22, s22, 0x1c200
	v_writelane_b32 v3, s22, 0
	s_add_u32 s22, s22, 0x10000
	v_writelane_b32 v3, s22, 1
	s_mul_i32 s22, s15, 0xe10
	v_writelane_b32 v3, s22, 2
	s_mul_i32 s22, s15, 0x4b0
	s_add_u32 s22, s22, 0x274200
	v_writelane_b32 v3, s22, 3
	s_mov_b64 exec, 15
	global_load_dword v93, v3, s[34:35]
	s_mov_b64 exec, s[18:19]
	s_branch .Lk1_back9
